# adds P8 padding rows of a block alias its first row (hot in cache)
# speedup vs baseline: 1.0040x; 1.0020x over previous
; #define LAS __attribute__((address_space(3)))
; #define PG8_STAGE(bufoff, gbase, voff) do { _Pragma("unroll") for (int _i = 0; _i < 2; ++_i) \
;         __builtin_amdgcn_global_load_lds((const unsigned*)((const char*)(gbase) + (voff)[_i]), (LAS unsigned*)(lds + (bufoff) + ldsw + _i * 8192), 16, 0, 0); } while (0)
; #define PG8_WAIT_V(n) asm volatile("s_waitcnt vmcnt(" #n ")" ::: "memory")
; #define PG8_BAR __builtin_amdgcn_s_barrier()
; template <class Epi, class Sched, bool GATHER, bool FP8>
; __device__ __forceinline__ void gemm_phase(LAS uchar* lds, const int K, const int LDA, const int LDB, const size_t kstepA, const size_t kstepB, const Sched& S, const Epi& E) {
;     ...
;     const char* cA = cur.pa; const char* cB = cur.pb;
;     if constexpr (GATHER) S.gather(cur, voA, (const LAS int*)nullptr);
;     PG8_STAGE(PG8_SB(0, 0), cB, voffB); PG8_STAGE(PG8_SB(0, 1), cB + hstep, voffB); PG8_STAGE(PG8_SA(0, 0), cA, voA[0]); PG8_STAGE(PG8_SA(0, 1), cA, voA[1]);
;     if (wr == 1) PG8_BAR;
;     PG8_WAIT_V(2); PG8_BAR;
;     PG8_STAGE(PG8_SB(1, 0), cB + kstepB, voffB); PG8_STAGE(PG8_SA(1, 0), cA + kstepA, voA[0]); PG8_STAGE(PG8_SB(1, 1), cB + hstep + kstepB, voffB);
;     __device__ __forceinline__ bool next(int i, pg8::Unit& u) const {
;         const int NB = __builtin_amdgcn_readfirstlane(tab[0]); const int L = i * G + c; if (L >= NB * nN) return false;
;         const int b = L / nN, pn = L - b * nN, e = __builtin_amdgcn_readfirstlane(tab[64 + b]);
;         u.pa = A; u.pb = B + (size_t)e * bexp + (size_t)pn * 256 * 128; u.row0 = b * 256; u.col0 = pn * 256; u.aux = e; u.blk = b; return true;
;     }
;     __device__ __forceinline__ void gather(const pg8::Unit& u, unsigned (&vo)[2][2], const LAS int*) const {
; #pragma unroll
;         for (int i = 0; i < 2; ++i) { int R, C; pg8::stage_rc((int)threadIdx.x * 16 + i * 8192, R, C);
; #pragma unroll
;             for (int h = 0; h < 2; ++h) vo[h][i] = (unsigned)(u.row0 + h * 128 + R) * (unsigned)W8LD + (unsigned)C * 2u; }
;     }
.Lsch8_done:
	s_barrier
	s_add_i32 s4, 0, 0x22000
	v_mov_b32_e32 v2, s4
	ds_read_b32 v2, v2
	v_readfirstlane_b32 s18, v0
	s_waitcnt lgkmcnt(0)
	v_readfirstlane_b32 s4, v2
	s_lshl_b32 s4, s4, 3
	v_mov_b32_e32 v3, 0x23c00
	ds_read_b32 v3, v3
	s_waitcnt lgkmcnt(0)
	v_readfirstlane_b32 s98, v3
	s_cmp_ge_i32 s98, s4
	s_cbranch_scc1 .LBB0_1041
	v_lshlrev_b32_e32 v3, 4, v0
	v_and_b32_e32 v2, 32, v0
	v_bitop3_b32 v2, v3, v2, 48 bitop3:0x6c
	v_or_b32_e32 v3, 0x2000, v3
	v_bfe_u32 v5, v0, 2, 4
	v_lshrrev_b32_e32 v6, 7, v3
	s_movk_i32 s8, 0x70
	s_add_u32 s4, s90, 0x1c000000
	v_and_or_b32 v216, v6, s8, v5
	v_lshrrev_b32_e32 v6, 5, v0
	s_addc_u32 s5, s91, 0
	v_and_or_b32 v195, v0, 64, v2
	v_and_b32_e32 v2, 48, v0
	v_and_b32_e32 v6, 4, v6
	v_bfe_u32 v7, v0, 2, 2
	s_add_u32 s23, s90, 0x50000000
	v_or3_b32 v6, v7, v6, v2
	v_lshrrev_b32_e32 v3, 6, v3
	s_movk_i32 s8, 0xc0
	s_addc_u32 s33, s91, 0
	v_and_or_b32 v3, v3, s8, v6
	s_ashr_i32 s8, s98, 31
	s_lshr_b32 s8, s8, 29
	s_add_i32 s8, s98, s8
	s_ashr_i32 s10, s8, 3
	s_lshl_b32 s9, s10, 2
	s_add_i32 s9, s9, 0
	s_add_i32 s9, s9, 0x22100
	v_lshl_or_b32 v196, v3, 7, v195
	v_mov_b32_e32 v3, s9
	ds_read_b32 v3, v3
	s_lshr_b32 s16, s18, 6
	s_and_b32 s8, s8, -8
	s_lshr_b32 s17, s18, 8
	s_lshl_b32 s44, s16, 10
	s_waitcnt lgkmcnt(0)
	v_readfirstlane_b32 s34, v3
	s_ashr_i32 s35, s34, 31
	s_sub_i32 s14, s98, s8
	s_lshl_b64 s[8:9], s[34:35], 22
	s_add_u32 s11, s23, s8
	s_addc_u32 s12, s33, s9
	s_ashr_i32 s15, s14, 31
	s_lshl_b64 s[8:9], s[14:15], 15
	v_lshrrev_b32_e32 v4, 2, v0
	s_add_u32 s36, s11, s8
	v_and_or_b32 v4, v4, 64, v6
	s_addc_u32 s37, s12, s9
	s_lshl_b32 s69, s10, 8
	s_lshl_b32 s100, s10, 2
	s_add_i32 s100, s100, 0x22400
	v_mov_b32_e32 v251, s100
	ds_read_b32 v251, v251
	s_waitcnt lgkmcnt(0)
	v_readfirstlane_b32 s100, v251
	v_lshl_or_b32 v198, v4, 7, v195
	s_movk_i32 s45, 0x80
	v_cmp_gt_i32_e32 vcc, s100, v216
	v_cndmask_b32_e32 v4, 0, v216, vcc
	v_or_b32_e32 v4, s69, v4
	v_mul_lo_u32 v4, v4, s45
	v_or_b32_e32 v219, 0x80, v216
	s_add_i32 s46, s44, 0
	v_or_b32_e32 v202, v4, v195
	v_cmp_gt_i32_e32 vcc, s100, v219
	v_cndmask_b32_e32 v4, 0, v219, vcc
	v_or_b32_e32 v4, s69, v4
	s_add_i32 s47, s46, 0x10000
	v_mov_b32_e32 v201, 0
	v_lshrrev_b32_e32 v3, 3, v0
	v_mul_lo_u32 v4, v4, s45
	v_mov_b32_e32 v199, v201
	s_mov_b32 m0, s47
	s_add_i32 s48, s46, 0x12000
	v_and_or_b32 v217, v3, 48, v5
	v_or_b32_e32 v204, v4, v195
	v_lshl_add_u64 v[4:5], s[36:37], 0, v[198:199]
	global_load_lds_dwordx4 v198, s[36:37]
	v_mov_b32_e32 v197, v201
	s_mov_b32 m0, s48
	s_add_i32 s49, s46, 0x14000
	s_mov_b64 s[8:9], 0x400
	v_cmp_gt_i32_e32 vcc, s100, v217
	v_cndmask_b32_e32 v3, 0, v217, vcc
	v_or_b32_e32 v3, s69, v3
	v_lshl_add_u64 v[6:7], s[36:37], 0, v[196:197]
	global_load_lds_dwordx4 v196, s[36:37]
	v_lshl_add_u64 v[4:5], v[4:5], 0, s[8:9]
	s_mov_b32 m0, s49
	s_add_i32 s50, s46, 0x16000
	v_mul_lo_u32 v3, v3, s45
	v_or_b32_e32 v218, 0x80, v217
	global_load_lds_dwordx4 v[4:5], off
	v_lshl_add_u64 v[4:5], v[6:7], 0, s[8:9]
	s_mov_b32 m0, s50
	v_or_b32_e32 v200, v3, v195
	v_cmp_gt_i32_e32 vcc, s100, v218
	v_cndmask_b32_e32 v3, 0, v218, vcc
	v_or_b32_e32 v3, s69, v3
	global_load_lds_dwordx4 v[4:5], off
	s_mov_b32 m0, s46
	s_add_i32 s51, s46, 0x2000
	v_mul_lo_u32 v3, v3, s45
	global_load_lds_dwordx4 v200, s[4:5]
	s_mov_b32 m0, s51
	s_add_i32 s52, s46, 0x4000
	v_or_b32_e32 v3, v3, v195
	global_load_lds_dwordx4 v202, s[4:5]
	s_mov_b32 m0, s52
	s_add_i32 s53, s46, 0x6000
	global_load_lds_dwordx4 v3, s[4:5]
	s_mov_b32 m0, s53
	s_load_dwordx2 s[10:11], s[0:1], 0x88
	global_load_lds_dwordx4 v204, s[4:5]
	s_cmp_eq_u32 s17, 1
	s_mov_b32 s54, 0x10000
	s_cselect_b64 s[12:13], -1, 0
	s_cmp_lg_u32 s17, 1
	v_mov_b32_e32 v203, v201
	s_cbranch_scc1 .LBB0_1025
	s_barrier

; #define LAS __attribute__((address_space(3)))
; #define PG8_BAR __builtin_amdgcn_s_barrier()
; template <class Epi, class Sched, bool GATHER, bool FP8>
; __device__ __forceinline__ void gemm_phase(LAS uchar* lds, const int K, const int LDA, const int LDB, const size_t kstepA, const size_t kstepB, const Sched& S, const Epi& E) {
;     ...
;         if (!has_next) break;
; #pragma unroll
;         for (int a = 0; a < 2; ++a)
; #pragma unroll
;             for (int b = 0; b < 2; ++b)
; #pragma unroll
;                 for (int m = 0; m < 4; ++m)
; #pragma unroll
;                     for (int n = 0; n < 2; ++n) acc[a][b][m][n] = (f32x4){0.f, 0.f, 0.f, 0.f};
;         cur = nxt; cA = nA; cB = nB; ++ui;
;         if (wr == 1) PG8_BAR;
;     __device__ __forceinline__ void gather(const pg8::Unit& u, unsigned (&vo)[2][2], const LAS int*) const {
; #pragma unroll
;         for (int i = 0; i < 2; ++i) { int R, C; pg8::stage_rc((int)threadIdx.x * 16 + i * 8192, R, C);
; #pragma unroll
;             for (int h = 0; h < 2; ++h) vo[h][i] = (unsigned)(u.row0 + h * 128 + R) * (unsigned)W8LD + (unsigned)C * 2u; }
;     }
.LBB0_1030:
	s_lshl_b32 s31, s38, 10
	s_and_b32 s31, s31, 0x400
	s_add_i32 s70, s31, 0
	s_ashr_i32 s35, s34, 31
	s_add_i32 s70, s70, 0x23400
	s_lshl_b64 s[34:35], s[34:35], 13
	s_add_u32 s39, s10, s34
	s_addc_u32 s40, s11, s35
	s_ashr_i32 s31, s30, 31
	s_lshl_b64 s[34:35], s[30:31], 2
	s_add_u32 s31, s39, s34
	s_addc_u32 s35, s40, s35
	s_add_u32 s34, s31, s62
	s_addc_u32 s35, s35, 0
	s_add_i32 m0, s70, s61
	s_lshr_b32 s100, s68, 6
	s_add_i32 s100, s100, 0x22400
	v_mov_b32_e32 v251, s100
	ds_read_b32 v251, v251
	s_waitcnt lgkmcnt(0)
	v_readfirstlane_b32 s100, v251
	v_cmp_gt_i32_e32 vcc, s100, v217
	v_cndmask_b32_e32 v2, 0, v217, vcc
	v_add_u32_e32 v2, s68, v2
	global_load_lds_dword v222, s[34:35]
	v_mul_lo_u32 v2, v2, s45
	v_or_b32_e32 v228, v2, v195
	v_cmp_gt_i32_e32 vcc, s100, v218
	v_cndmask_b32_e32 v2, 0, v218, vcc
	v_add_u32_e32 v2, s68, v2
	v_mul_lo_u32 v2, v2, s45
	v_or_b32_e32 v208, v2, v195
	v_cmp_gt_i32_e32 vcc, s100, v216
	v_cndmask_b32_e32 v2, 0, v216, vcc
	v_add_u32_e32 v2, s68, v2
	v_mul_lo_u32 v2, v2, s45
	s_cmp_lg_u32 s38, 0
	v_or_b32_e32 v229, v2, v195
	v_cmp_gt_i32_e32 vcc, s100, v219
	v_cndmask_b32_e32 v2, 0, v219, vcc
	v_add_u32_e32 v2, s68, v2
	s_cselect_b64 s[34:35], -1, 0
	v_mul_lo_u32 v2, v2, s45
	s_add_u32 s31, s36, 0x80000
	v_mov_b32_e32 v66, 0
	v_or_b32_e32 v210, v2, v195
	v_mov_b32_e32 v209, v201
	v_mov_b32_e32 v211, v201
	s_addc_u32 s71, s37, 0
	s_mov_b32 s72, -2
	s_mov_b64 s[36:37], 0
	v_mov_b32_e32 v67, v66
	v_mov_b32_e32 v68, v66
	v_mov_b32_e32 v69, v66
	v_mov_b32_e32 v70, v66
	v_mov_b32_e32 v71, v66
	v_mov_b32_e32 v72, v66
	v_mov_b32_e32 v73, v66
	v_mov_b32_e32 v82, v66
	v_mov_b32_e32 v83, v66
	v_mov_b32_e32 v84, v66
	v_mov_b32_e32 v85, v66
	v_mov_b32_e32 v86, v66
	v_mov_b32_e32 v87, v66
	v_mov_b32_e32 v88, v66
	v_mov_b32_e32 v89, v66
	v_mov_b32_e32 v98, v66
	v_mov_b32_e32 v99, v66
	v_mov_b32_e32 v100, v66
	v_mov_b32_e32 v101, v66
	v_mov_b32_e32 v102, v66
	v_mov_b32_e32 v103, v66
	v_mov_b32_e32 v104, v66
	v_mov_b32_e32 v105, v66
	v_mov_b32_e32 v114, v66
	v_mov_b32_e32 v115, v66
	v_mov_b32_e32 v116, v66
	v_mov_b32_e32 v117, v66
	v_mov_b32_e32 v118, v66
	v_mov_b32_e32 v119, v66
	v_mov_b32_e32 v120, v66
	v_mov_b32_e32 v121, v66
	v_mov_b32_e32 v74, v66
	v_mov_b32_e32 v75, v66
	v_mov_b32_e32 v76, v66
	v_mov_b32_e32 v77, v66
	v_mov_b32_e32 v78, v66
	v_mov_b32_e32 v79, v66
	v_mov_b32_e32 v80, v66
	v_mov_b32_e32 v81, v66
	v_mov_b32_e32 v90, v66
	v_mov_b32_e32 v91, v66
	v_mov_b32_e32 v92, v66
	v_mov_b32_e32 v93, v66
	v_mov_b32_e32 v94, v66
	v_mov_b32_e32 v95, v66
	v_mov_b32_e32 v96, v66
	v_mov_b32_e32 v97, v66
	v_mov_b32_e32 v106, v66
	v_mov_b32_e32 v107, v66
	v_mov_b32_e32 v108, v66
	v_mov_b32_e32 v109, v66
	v_mov_b32_e32 v110, v66
	v_mov_b32_e32 v111, v66
	v_mov_b32_e32 v112, v66
	v_mov_b32_e32 v113, v66
	v_mov_b32_e32 v122, v66
	v_mov_b32_e32 v123, v66
	v_mov_b32_e32 v124, v66
	v_mov_b32_e32 v125, v66
	v_mov_b32_e32 v126, v66
	v_mov_b32_e32 v127, v66
	v_mov_b32_e32 v128, v66
	v_mov_b32_e32 v129, v66
	v_mov_b32_e32 v130, v66
	v_mov_b32_e32 v131, v66
	v_mov_b32_e32 v132, v66
	v_mov_b32_e32 v133, v66
	v_mov_b32_e32 v134, v66
	v_mov_b32_e32 v135, v66
	v_mov_b32_e32 v136, v66
	v_mov_b32_e32 v137, v66
	v_mov_b32_e32 v146, v66
	v_mov_b32_e32 v147, v66
	v_mov_b32_e32 v148, v66
	v_mov_b32_e32 v149, v66
	v_mov_b32_e32 v150, v66
	v_mov_b32_e32 v151, v66
	v_mov_b32_e32 v152, v66
	v_mov_b32_e32 v153, v66
	v_mov_b32_e32 v162, v66
	v_mov_b32_e32 v163, v66
	v_mov_b32_e32 v164, v66
	v_mov_b32_e32 v165, v66
	v_mov_b32_e32 v166, v66
	v_mov_b32_e32 v167, v66
	v_mov_b32_e32 v168, v66
	v_mov_b32_e32 v169, v66
	v_mov_b32_e32 v178, v66
	v_mov_b32_e32 v179, v66
	v_mov_b32_e32 v180, v66
	v_mov_b32_e32 v181, v66
	v_mov_b32_e32 v182, v66
	v_mov_b32_e32 v183, v66
	v_mov_b32_e32 v184, v66
	v_mov_b32_e32 v185, v66
	v_mov_b32_e32 v138, v66
	v_mov_b32_e32 v139, v66
	v_mov_b32_e32 v140, v66
	v_mov_b32_e32 v141, v66
	v_mov_b32_e32 v142, v66
	v_mov_b32_e32 v143, v66
	v_mov_b32_e32 v144, v66
	v_mov_b32_e32 v145, v66
	v_mov_b32_e32 v154, v66
	v_mov_b32_e32 v155, v66
	v_mov_b32_e32 v156, v66
	v_mov_b32_e32 v157, v66
	v_mov_b32_e32 v158, v66
	v_mov_b32_e32 v159, v66
	v_mov_b32_e32 v160, v66
	v_mov_b32_e32 v161, v66
	v_mov_b32_e32 v170, v66
	v_mov_b32_e32 v171, v66
	v_mov_b32_e32 v172, v66
	v_mov_b32_e32 v173, v66
	v_mov_b32_e32 v174, v66
	v_mov_b32_e32 v175, v66
	v_mov_b32_e32 v176, v66
	v_mov_b32_e32 v177, v66
	v_mov_b32_e32 v186, v66
	v_mov_b32_e32 v187, v66
	v_mov_b32_e32 v188, v66
	v_mov_b32_e32 v189, v66
	v_mov_b32_e32 v190, v66
	v_mov_b32_e32 v191, v66
	v_mov_b32_e32 v192, v66
	v_mov_b32_e32 v193, v66
	s_branch .LBB0_1033
